# P5: the last head of a unit no longer issues the (unused) next-head z loads
# baseline (speedup 1.0000x reference)
.Lp5_z0skip:
	s_cmpk_eq_i32 s0, 0x700
	s_cbranch_scc1 .Lp5_pf_skip
	global_load_dwordx4 v[200:203], v[198:199], off offset:128
	global_load_dwordx4 v[216:219], v[198:199], off offset:192
	global_load_dword v2, v124, s[92:93]
	global_load_dword v1, v122, s[92:93]
	global_load_dword v12, v120, s[92:93]
	s_add_u32 s4, s92, 0x45c00000
	s_addc_u32 s5, s93, 0
	global_load_dword v3, v118, s[4:5] offset:128
	s_add_u32 s4, s4, 0x3000
	s_addc_u32 s5, s5, 0
	global_load_dword v4, v118, s[4:5] offset:128
	s_add_u32 s4, s4, 0x3000
	s_addc_u32 s5, s5, 0
	global_load_dword v5, v118, s[4:5] offset:128
	s_add_u32 s4, s4, 0x3000
	s_addc_u32 s5, s5, 0
	global_load_dword v6, v118, s[4:5] offset:128
	s_add_u32 s4, s4, 0x3000
	s_addc_u32 s5, s5, 0
	global_load_dword v7, v118, s[4:5] offset:128
	s_add_u32 s4, s4, 0x3000
	s_addc_u32 s5, s5, 0
	global_load_dword v8, v118, s[4:5] offset:128
	s_add_u32 s4, s4, 0x3000
	s_addc_u32 s5, s5, 0
	global_load_dword v9, v118, s[4:5] offset:128
	global_load_dword v10, v116, s[92:93]
	s_mov_b32 s5, 0
	v_lshl_add_u64 v[94:95], s[92:93], 0, v[114:115]
	s_mov_b32 s4, 0x5e004000
	v_lshl_add_u64 v[16:17], v[94:95], 0, s[4:5]
	global_load_dwordx4 v[14:17], v[16:17], off
	s_mov_b32 s4, 0x5e006000
	v_lshl_add_u64 v[18:19], v[94:95], 0, s[4:5]
	global_load_dwordx4 v[18:21], v[18:19], off
